# gemm0+gemm1: both wave halves run their unit epilogue in the same barrier interval (extra barrier before leading half's epilogue, after trailing half's)
# speedup vs baseline: 1.0055x; 1.0055x over previous
.LBB2_8:
	s_cmpk_gt_u32 s3, 0xff
	s_cbranch_scc1 .Lus_g0_a
	s_barrier
.Lus_g0_a:
	s_cmp_lt_i32 s61, 5
	s_cselect_b64 vcc, -1, 0
	v_lshl_or_b32 v142, s61, 8, v144
	v_cndmask_b32_e32 v140, 1.0, v148, vcc
	v_lshl_add_u32 v149, s62, 8, v1
	v_ashrrev_i32_e32 v143, 31, v142
	v_lshl_add_u64 v[142:143], v[142:143], 1, s[20:21]
	v_mad_i64_i32 v[150:151], s[26:27], v149, s56, 0
	v_pk_mul_f32 v[128:129], v[140:141], v[128:129] op_sel_hi:[0,1]
	v_pk_mul_f32 v[126:127], v[140:141], v[126:127] op_sel_hi:[0,1]
	v_pk_mul_f32 v[152:153], v[140:141], v[124:125] op_sel_hi:[0,1]
	v_pk_mul_f32 v[124:125], v[140:141], v[122:123] op_sel_hi:[0,1]
	v_lshl_add_u64 v[150:151], v[150:151], 1, v[142:143]
	v_cvt_pk_f16_f32 v122, v126, v127
	v_cvt_pk_f16_f32 v123, v128, v129
	v_cvt_pk_f16_f32 v124, v124, v125
	v_cvt_pk_f16_f32 v125, v152, v153
	global_store_dwordx4 v[150:151], v[122:125], off
	v_pk_mul_f32 v[120:121], v[140:141], v[120:121] op_sel_hi:[0,1]
	v_pk_mul_f32 v[118:119], v[140:141], v[118:119] op_sel_hi:[0,1]
	v_pk_mul_f32 v[122:123], v[140:141], v[116:117] op_sel_hi:[0,1]
	v_pk_mul_f32 v[116:117], v[140:141], v[114:115] op_sel_hi:[0,1]
	v_cvt_pk_f16_f32 v114, v118, v119
	v_cvt_pk_f16_f32 v115, v120, v121
	v_cvt_pk_f16_f32 v116, v116, v117
	v_cvt_pk_f16_f32 v117, v122, v123
	global_store_dwordx4 v[150:151], v[114:117], off offset:256
	v_pk_mul_f32 v[112:113], v[140:141], v[112:113] op_sel_hi:[0,1]
	v_pk_mul_f32 v[110:111], v[140:141], v[110:111] op_sel_hi:[0,1]
	v_or_b32_e32 v114, 16, v149
	v_mad_i64_i32 v[114:115], s[26:27], v114, s56, 0
	v_pk_mul_f32 v[116:117], v[140:141], v[108:109] op_sel_hi:[0,1]
	v_pk_mul_f32 v[108:109], v[140:141], v[106:107] op_sel_hi:[0,1]
	v_lshl_add_u64 v[114:115], v[114:115], 1, v[142:143]
	v_cvt_pk_f16_f32 v106, v110, v111
	v_cvt_pk_f16_f32 v107, v112, v113
	v_cvt_pk_f16_f32 v108, v108, v109
	v_cvt_pk_f16_f32 v109, v116, v117
	global_store_dwordx4 v[114:115], v[106:109], off
	v_pk_mul_f32 v[104:105], v[140:141], v[104:105] op_sel_hi:[0,1]
	v_pk_mul_f32 v[102:103], v[140:141], v[102:103] op_sel_hi:[0,1]
	v_pk_mul_f32 v[106:107], v[140:141], v[100:101] op_sel_hi:[0,1]
	v_pk_mul_f32 v[100:101], v[140:141], v[98:99] op_sel_hi:[0,1]
	v_cvt_pk_f16_f32 v98, v102, v103
	v_cvt_pk_f16_f32 v99, v104, v105
	v_cvt_pk_f16_f32 v100, v100, v101
	v_cvt_pk_f16_f32 v101, v106, v107
	global_store_dwordx4 v[114:115], v[98:101], off offset:256
	v_pk_mul_f32 v[96:97], v[140:141], v[96:97] op_sel_hi:[0,1]
	v_pk_mul_f32 v[94:95], v[140:141], v[94:95] op_sel_hi:[0,1]
	v_or_b32_e32 v98, 32, v149
	v_mad_i64_i32 v[98:99], s[26:27], v98, s56, 0
	v_pk_mul_f32 v[100:101], v[140:141], v[92:93] op_sel_hi:[0,1]
	v_pk_mul_f32 v[92:93], v[140:141], v[90:91] op_sel_hi:[0,1]
	v_lshl_add_u64 v[98:99], v[98:99], 1, v[142:143]
	v_cvt_pk_f16_f32 v90, v94, v95
	v_cvt_pk_f16_f32 v91, v96, v97
	v_cvt_pk_f16_f32 v92, v92, v93
	v_cvt_pk_f16_f32 v93, v100, v101
	global_store_dwordx4 v[98:99], v[90:93], off
	v_pk_mul_f32 v[88:89], v[140:141], v[88:89] op_sel_hi:[0,1]
	v_pk_mul_f32 v[86:87], v[140:141], v[86:87] op_sel_hi:[0,1]
	v_pk_mul_f32 v[90:91], v[140:141], v[84:85] op_sel_hi:[0,1]
	v_pk_mul_f32 v[84:85], v[140:141], v[82:83] op_sel_hi:[0,1]
	v_cvt_pk_f16_f32 v82, v86, v87
	v_cvt_pk_f16_f32 v83, v88, v89
	v_cvt_pk_f16_f32 v84, v84, v85
	v_cvt_pk_f16_f32 v85, v90, v91
	global_store_dwordx4 v[98:99], v[82:85], off offset:256
	v_pk_mul_f32 v[80:81], v[140:141], v[80:81] op_sel_hi:[0,1]
	v_pk_mul_f32 v[78:79], v[140:141], v[78:79] op_sel_hi:[0,1]
	v_or_b32_e32 v82, 48, v149
	v_mad_i64_i32 v[82:83], s[26:27], v82, s56, 0
	v_pk_mul_f32 v[84:85], v[140:141], v[76:77] op_sel_hi:[0,1]
	v_pk_mul_f32 v[76:77], v[140:141], v[74:75] op_sel_hi:[0,1]
	v_lshl_add_u64 v[82:83], v[82:83], 1, v[142:143]
	v_cvt_pk_f16_f32 v74, v78, v79
	v_cvt_pk_f16_f32 v75, v80, v81
	v_cvt_pk_f16_f32 v76, v76, v77
	v_cvt_pk_f16_f32 v77, v84, v85
	global_store_dwordx4 v[82:83], v[74:77], off
	v_pk_mul_f32 v[72:73], v[140:141], v[72:73] op_sel_hi:[0,1]
	v_pk_mul_f32 v[70:71], v[140:141], v[70:71] op_sel_hi:[0,1]
	v_pk_mul_f32 v[74:75], v[140:141], v[68:69] op_sel_hi:[0,1]
	v_pk_mul_f32 v[68:69], v[140:141], v[66:67] op_sel_hi:[0,1]
	v_cvt_pk_f16_f32 v66, v70, v71
	v_cvt_pk_f16_f32 v67, v72, v73
	v_cvt_pk_f16_f32 v68, v68, v69
	v_cvt_pk_f16_f32 v69, v74, v75
	global_store_dwordx4 v[82:83], v[66:69], off offset:256
	v_pk_mul_f32 v[64:65], v[140:141], v[64:65] op_sel_hi:[0,1]
	v_pk_mul_f32 v[62:63], v[140:141], v[62:63] op_sel_hi:[0,1]
	v_add_u32_e32 v66, 0x80, v149
	v_mad_i64_i32 v[66:67], s[26:27], v66, s56, 0
	v_pk_mul_f32 v[68:69], v[140:141], v[60:61] op_sel_hi:[0,1]
	v_pk_mul_f32 v[60:61], v[140:141], v[58:59] op_sel_hi:[0,1]
	v_lshl_add_u64 v[66:67], v[66:67], 1, v[142:143]
	v_cvt_pk_f16_f32 v58, v62, v63
	v_cvt_pk_f16_f32 v59, v64, v65
	v_cvt_pk_f16_f32 v60, v60, v61
	v_cvt_pk_f16_f32 v61, v68, v69
	global_store_dwordx4 v[66:67], v[58:61], off
	v_pk_mul_f32 v[56:57], v[140:141], v[56:57] op_sel_hi:[0,1]
	v_pk_mul_f32 v[54:55], v[140:141], v[54:55] op_sel_hi:[0,1]
	v_pk_mul_f32 v[58:59], v[140:141], v[52:53] op_sel_hi:[0,1]
	v_pk_mul_f32 v[52:53], v[140:141], v[50:51] op_sel_hi:[0,1]
	v_cvt_pk_f16_f32 v50, v54, v55
	v_cvt_pk_f16_f32 v51, v56, v57
	v_cvt_pk_f16_f32 v52, v52, v53
	v_cvt_pk_f16_f32 v53, v58, v59
	global_store_dwordx4 v[66:67], v[50:53], off offset:256
	v_pk_mul_f32 v[48:49], v[140:141], v[48:49] op_sel_hi:[0,1]
	v_pk_mul_f32 v[46:47], v[140:141], v[46:47] op_sel_hi:[0,1]
	v_add_u32_e32 v50, 0x90, v149
	v_mad_i64_i32 v[50:51], s[26:27], v50, s56, 0
	v_pk_mul_f32 v[52:53], v[140:141], v[44:45] op_sel_hi:[0,1]
	v_pk_mul_f32 v[44:45], v[140:141], v[42:43] op_sel_hi:[0,1]
	v_lshl_add_u64 v[50:51], v[50:51], 1, v[142:143]
	v_cvt_pk_f16_f32 v42, v46, v47
	v_cvt_pk_f16_f32 v43, v48, v49
	v_cvt_pk_f16_f32 v44, v44, v45
	v_cvt_pk_f16_f32 v45, v52, v53
	global_store_dwordx4 v[50:51], v[42:45], off
	v_pk_mul_f32 v[40:41], v[140:141], v[40:41] op_sel_hi:[0,1]
	v_pk_mul_f32 v[38:39], v[140:141], v[38:39] op_sel_hi:[0,1]
	v_pk_mul_f32 v[42:43], v[140:141], v[36:37] op_sel_hi:[0,1]
	v_pk_mul_f32 v[36:37], v[140:141], v[34:35] op_sel_hi:[0,1]
	v_cvt_pk_f16_f32 v34, v38, v39
	v_cvt_pk_f16_f32 v35, v40, v41
	v_cvt_pk_f16_f32 v36, v36, v37
	v_cvt_pk_f16_f32 v37, v42, v43
	global_store_dwordx4 v[50:51], v[34:37], off offset:256
	v_pk_mul_f32 v[32:33], v[140:141], v[32:33] op_sel_hi:[0,1]
	v_pk_mul_f32 v[30:31], v[140:141], v[30:31] op_sel_hi:[0,1]
	v_add_u32_e32 v34, 0xa0, v149
	v_mad_i64_i32 v[34:35], s[26:27], v34, s56, 0
	v_pk_mul_f32 v[36:37], v[140:141], v[28:29] op_sel_hi:[0,1]
	v_pk_mul_f32 v[28:29], v[140:141], v[26:27] op_sel_hi:[0,1]
	v_lshl_add_u64 v[34:35], v[34:35], 1, v[142:143]
	v_cvt_pk_f16_f32 v26, v30, v31
	v_cvt_pk_f16_f32 v27, v32, v33
	v_cvt_pk_f16_f32 v28, v28, v29
	v_cvt_pk_f16_f32 v29, v36, v37
	global_store_dwordx4 v[34:35], v[26:29], off
	v_pk_mul_f32 v[24:25], v[140:141], v[24:25] op_sel_hi:[0,1]
	v_pk_mul_f32 v[22:23], v[140:141], v[22:23] op_sel_hi:[0,1]
	v_pk_mul_f32 v[26:27], v[140:141], v[20:21] op_sel_hi:[0,1]
	v_pk_mul_f32 v[20:21], v[140:141], v[18:19] op_sel_hi:[0,1]
	v_cvt_pk_f16_f32 v18, v22, v23
	v_cvt_pk_f16_f32 v19, v24, v25
	v_cvt_pk_f16_f32 v20, v20, v21
	v_cvt_pk_f16_f32 v21, v26, v27
	global_store_dwordx4 v[34:35], v[18:21], off offset:256
	v_pk_mul_f32 v[16:17], v[140:141], v[16:17] op_sel_hi:[0,1]
	v_pk_mul_f32 v[14:15], v[140:141], v[14:15] op_sel_hi:[0,1]
	v_add_u32_e32 v18, 0xb0, v149
	v_mad_i64_i32 v[18:19], s[26:27], v18, s56, 0
	v_pk_mul_f32 v[20:21], v[140:141], v[12:13] op_sel_hi:[0,1]
	v_pk_mul_f32 v[12:13], v[140:141], v[10:11] op_sel_hi:[0,1]
	v_lshl_add_u64 v[18:19], v[18:19], 1, v[142:143]
	v_cvt_pk_f16_f32 v10, v14, v15
	v_cvt_pk_f16_f32 v11, v16, v17
	v_cvt_pk_f16_f32 v12, v12, v13
	v_cvt_pk_f16_f32 v13, v20, v21
	global_store_dwordx4 v[18:19], v[10:13], off
	v_pk_mul_f32 v[8:9], v[140:141], v[8:9] op_sel_hi:[0,1]
	v_pk_mul_f32 v[6:7], v[140:141], v[6:7] op_sel_hi:[0,1]
	v_pk_mul_f32 v[10:11], v[140:141], v[4:5] op_sel_hi:[0,1]
	v_pk_mul_f32 v[4:5], v[140:141], v[2:3] op_sel_hi:[0,1]
	v_cvt_pk_f16_f32 v2, v6, v7
	v_cvt_pk_f16_f32 v3, v8, v9
	v_cvt_pk_f16_f32 v4, v4, v5
	v_cvt_pk_f16_f32 v5, v10, v11
	s_and_b64 vcc, exec, s[8:9]
	s_mov_b32 s62, s60
	s_mov_b32 s61, s59
	s_mov_b64 s[26:27], s[6:7]
	s_mov_b64 s[28:29], s[4:5]
	global_store_dwordx4 v[18:19], v[2:5], off offset:256
	s_cmpk_gt_u32 s3, 0xff
	s_cbranch_scc0 .Lus_g0_b
	s_barrier
.Lus_g0_b:
	s_cbranch_vccnz .LBB2_22

.LBB3_10:
	s_cmpk_gt_u32 s41, 0xff
	s_cbranch_scc1 .Lus_g1_a
	s_barrier
.Lus_g1_a:
	v_lshl_or_b32 v128, s68, 8, v168
	v_ashrrev_i32_e32 v129, 31, v128
	v_lshlrev_b64 v[154:155], 2, v[128:129]
	v_lshl_add_u64 v[128:129], s[10:11], 0, v[154:155]
	global_load_dwordx4 v[140:143], v[128:129], off
	global_load_dwordx4 v[136:139], v[128:129], off offset:64
	global_load_dwordx4 v[132:135], v[128:129], off offset:512
	s_nop 0
	global_load_dwordx4 v[128:131], v[128:129], off offset:576
	v_lshl_add_u32 v180, s67, 8, v167
	v_add_u32_e32 v178, 0x80, v180
	v_mad_i64_i32 v[156:157], s[30:31], v180, s42, 0
	v_or_b32_e32 v172, 16, v180
	v_or_b32_e32 v174, 32, v180
	v_or_b32_e32 v176, 48, v180
	v_mad_i64_i32 v[178:179], s[30:31], v178, s42, 0
	v_lshl_add_u64 v[154:155], s[8:9], 0, v[154:155]
	v_mad_i64_i32 v[172:173], s[30:31], v172, s42, 0
	v_mad_i64_i32 v[174:175], s[30:31], v174, s42, 0
	v_mad_i64_i32 v[176:177], s[30:31], v176, s42, 0
	v_lshl_add_u64 v[156:157], v[156:157], 2, v[154:155]
	v_lshl_add_u64 v[178:179], v[178:179], 2, v[154:155]
	v_lshl_add_u64 v[172:173], v[172:173], 2, v[154:155]
	v_lshl_add_u64 v[174:175], v[174:175], 2, v[154:155]
	v_lshl_add_u64 v[176:177], v[176:177], 2, v[154:155]
	s_mov_b32 s67, s66
	s_mov_b32 s68, s65
	s_mov_b64 s[34:35], s[28:29]
	s_mov_b64 vcc, s[0:1]
	s_waitcnt vmcnt(0)
	v_pk_add_f32 v[118:119], v[142:143], v[118:119]
	v_pk_add_f32 v[116:117], v[140:141], v[116:117]
	v_pk_add_f32 v[126:127], v[138:139], v[126:127]
	v_pk_add_f32 v[50:51], v[130:131], v[50:51]
	v_pk_add_f32 v[48:49], v[128:129], v[48:49]
	v_pk_add_f32 v[124:125], v[136:137], v[124:125]
	v_pk_add_f32 v[122:123], v[134:135], v[122:123]
	v_pk_add_f32 v[120:121], v[132:133], v[120:121]
	v_pk_add_f32 v[114:115], v[130:131], v[114:115]
	v_pk_add_f32 v[112:113], v[128:129], v[112:113]
	v_pk_add_f32 v[110:111], v[142:143], v[110:111]
	v_pk_add_f32 v[108:109], v[140:141], v[108:109]
	v_pk_add_f32 v[106:107], v[138:139], v[106:107]
	v_pk_add_f32 v[104:105], v[136:137], v[104:105]
	v_pk_add_f32 v[102:103], v[134:135], v[102:103]
	v_pk_add_f32 v[100:101], v[132:133], v[100:101]
	v_pk_add_f32 v[98:99], v[130:131], v[98:99]
	v_pk_add_f32 v[96:97], v[128:129], v[96:97]
	v_pk_add_f32 v[94:95], v[142:143], v[94:95]
	v_pk_add_f32 v[92:93], v[140:141], v[92:93]
	v_pk_add_f32 v[90:91], v[138:139], v[90:91]
	v_pk_add_f32 v[88:89], v[136:137], v[88:89]
	v_pk_add_f32 v[86:87], v[134:135], v[86:87]
	v_pk_add_f32 v[84:85], v[132:133], v[84:85]
	v_pk_add_f32 v[82:83], v[130:131], v[82:83]
	v_pk_add_f32 v[80:81], v[128:129], v[80:81]
	v_pk_add_f32 v[78:79], v[142:143], v[78:79]
	v_pk_add_f32 v[76:77], v[140:141], v[76:77]
	v_pk_add_f32 v[74:75], v[138:139], v[74:75]
	v_pk_add_f32 v[72:73], v[136:137], v[72:73]
	v_pk_add_f32 v[70:71], v[134:135], v[70:71]
	v_pk_add_f32 v[68:69], v[132:133], v[68:69]
	v_pk_add_f32 v[66:67], v[130:131], v[66:67]
	v_pk_add_f32 v[64:65], v[128:129], v[64:65]
	v_pk_add_f32 v[62:63], v[142:143], v[62:63]
	v_pk_add_f32 v[60:61], v[140:141], v[60:61]
	v_pk_add_f32 v[58:59], v[138:139], v[58:59]
	v_pk_add_f32 v[56:57], v[136:137], v[56:57]
	v_pk_add_f32 v[54:55], v[134:135], v[54:55]
	v_pk_add_f32 v[52:53], v[132:133], v[52:53]
	global_store_dwordx4 v[156:157], v[116:119], off
	global_store_dwordx4 v[156:157], v[124:127], off offset:64
	global_store_dwordx4 v[156:157], v[120:123], off offset:512
	global_store_dwordx4 v[156:157], v[112:115], off offset:576
	global_store_dwordx4 v[172:173], v[108:111], off
	global_store_dwordx4 v[172:173], v[104:107], off offset:64
	global_store_dwordx4 v[172:173], v[100:103], off offset:512
	global_store_dwordx4 v[172:173], v[96:99], off offset:576
	global_store_dwordx4 v[174:175], v[92:95], off
	global_store_dwordx4 v[174:175], v[88:91], off offset:64
	global_store_dwordx4 v[174:175], v[84:87], off offset:512
	global_store_dwordx4 v[174:175], v[80:83], off offset:576
	global_store_dwordx4 v[176:177], v[76:79], off
	global_store_dwordx4 v[176:177], v[72:75], off offset:64
	global_store_dwordx4 v[176:177], v[68:71], off offset:512
	global_store_dwordx4 v[176:177], v[64:67], off offset:576
	global_store_dwordx4 v[178:179], v[60:63], off
	global_store_dwordx4 v[178:179], v[56:59], off offset:64
	global_store_dwordx4 v[178:179], v[52:55], off offset:512
	global_store_dwordx4 v[178:179], v[48:51], off offset:576
	v_pk_add_f32 v[34:35], v[130:131], v[34:35]
	v_pk_add_f32 v[32:33], v[128:129], v[32:33]
	v_add_u32_e32 v48, 0x90, v180
	v_mad_i64_i32 v[48:49], s[30:31], v48, s42, 0
	v_lshl_add_u64 v[48:49], v[48:49], 2, v[154:155]
	global_store_dwordx4 v[48:49], v[32:35], off offset:576
	v_pk_add_f32 v[46:47], v[142:143], v[46:47]
	v_pk_add_f32 v[44:45], v[140:141], v[44:45]
	v_add_u32_e32 v32, 0xa0, v180
	v_mad_i64_i32 v[32:33], s[30:31], v32, s42, 0
	v_pk_add_f32 v[42:43], v[138:139], v[42:43]
	v_pk_add_f32 v[40:41], v[136:137], v[40:41]
	v_pk_add_f32 v[38:39], v[134:135], v[38:39]
	v_pk_add_f32 v[36:37], v[132:133], v[36:37]
	v_lshl_add_u64 v[32:33], v[32:33], 2, v[154:155]
	v_pk_add_f32 v[18:19], v[130:131], v[18:19]
	v_pk_add_f32 v[16:17], v[128:129], v[16:17]
	global_store_dwordx4 v[48:49], v[44:47], off
	global_store_dwordx4 v[48:49], v[40:43], off offset:64
	global_store_dwordx4 v[48:49], v[36:39], off offset:512
	global_store_dwordx4 v[32:33], v[16:19], off offset:576
	v_pk_add_f32 v[30:31], v[142:143], v[30:31]
	v_pk_add_f32 v[28:29], v[140:141], v[28:29]
	v_add_u32_e32 v16, 0xb0, v180
	v_mad_i64_i32 v[16:17], s[30:31], v16, s42, 0
	v_pk_add_f32 v[26:27], v[138:139], v[26:27]
	v_pk_add_f32 v[24:25], v[136:137], v[24:25]
	v_pk_add_f32 v[22:23], v[134:135], v[22:23]
	v_pk_add_f32 v[20:21], v[132:133], v[20:21]
	v_lshl_add_u64 v[16:17], v[16:17], 2, v[154:155]
	v_pk_add_f32 v[14:15], v[142:143], v[14:15]
	v_pk_add_f32 v[12:13], v[140:141], v[12:13]
	v_pk_add_f32 v[10:11], v[138:139], v[10:11]
	v_pk_add_f32 v[8:9], v[136:137], v[8:9]
	v_pk_add_f32 v[6:7], v[134:135], v[6:7]
	v_pk_add_f32 v[4:5], v[132:133], v[4:5]
	v_pk_add_f32 v[2:3], v[130:131], v[2:3]
	v_pk_add_f32 v[0:1], v[128:129], v[0:1]
	s_mov_b64 s[30:31], s[4:5]
	global_store_dwordx4 v[32:33], v[28:31], off
	global_store_dwordx4 v[32:33], v[24:27], off offset:64
	global_store_dwordx4 v[32:33], v[20:23], off offset:512
	global_store_dwordx4 v[16:17], v[12:15], off
	global_store_dwordx4 v[16:17], v[8:11], off offset:64
	global_store_dwordx4 v[16:17], v[4:7], off offset:512
	global_store_dwordx4 v[16:17], v[0:3], off offset:576
	s_cmpk_gt_u32 s41, 0xff
	s_cbranch_scc0 .Lus_g1_b
	s_barrier
